# w2 fp8 conversion of layers 1-3 moved from the prologue into the epilogues of expert GEMM 1 of the previous layer (first 8 units per workgroup)
# speedup vs baseline: 1.0387x; 1.0011x over previous
.LBB0_10:
	s_cmpk_gt_i32 s73, 0x9ff
	s_mov_b64 s[4:5], -1
	s_cbranch_scc0 .LBB0_89
	s_cmpk_gt_u32 s73, 0x1dff
	s_cbranch_scc0 .LBB0_21
	s_cmpk_gt_u32 s73, 0x21ff
	s_cbranch_scc0 .LBB0_18
	s_cmp_gt_u32 s73, 0x121ff
	s_cbranch_scc0 .LBB0_15
	s_cmpk_lg_i32 s16, 0x800
	s_cbranch_scc1 .Lp0_w2_do
	s_cmp_gt_u32 s73, 0x141ff
	s_cbranch_scc1 .Lp0_w2_skip
.Lp0_w2_do:
	s_add_i32 s4, s73, 0xfffede00
	s_lshr_b32 s22, s4, 8
	s_lshl_b64 s[24:25], s[22:23], 20
	s_lshl_b64 s[4:5], s[22:23], 22
	s_add_u32 s51, s20, s4
	s_addc_u32 s55, s21, s5
	s_add_u32 s5, s15, s24
	s_addc_u32 s22, s17, s25
	s_and_b32 s4, s41, 0x3e0
	s_and_b32 s25, s73, 0xe0
	s_and_b32 s24, s39, 0x380
	v_or_b32_e32 v2, s25, v1
	s_lshl_b32 s25, s4, 2
	s_add_u32 s74, s51, s25
	s_addc_u32 s75, s55, 0
	v_lshlrev_b32_e32 v2, 14, v2
	v_lshl_add_u64 v[4:5], s[74:75], 0, v[70:71]
	v_mov_b32_e32 v3, v71
	v_lshl_add_u64 v[50:51], v[4:5], 0, v[2:3]
	v_add_co_u32_e32 v10, vcc, s47, v50
	global_load_dwordx4 v[2:5], v[50:51], off nt
	s_nop 0
	v_addc_co_u32_e32 v11, vcc, 0, v51, vcc
	v_add_co_u32_e32 v14, vcc, s48, v50
	global_load_dwordx4 v[6:9], v[10:11], off offset:-4096 nt
	s_nop 0
	global_load_dwordx4 v[10:13], v[10:11], off nt
	v_addc_co_u32_e32 v15, vcc, 0, v51, vcc
	v_add_co_u32_e32 v22, vcc, s49, v50
	global_load_dwordx4 v[14:17], v[14:15], off nt
	s_nop 0
	v_addc_co_u32_e32 v23, vcc, 0, v51, vcc
	global_load_dwordx4 v[18:21], v[22:23], off offset:-4096 nt
	s_nop 0
	global_load_dwordx4 v[22:25], v[22:23], off nt
	v_add_co_u32_e32 v30, vcc, s50, v50
	v_mov_b32_e32 v76, v71
	s_nop 0
	v_addc_co_u32_e32 v31, vcc, 0, v51, vcc
	global_load_dwordx4 v[26:29], v[30:31], off offset:-4096 nt
	s_nop 0
	global_load_dwordx4 v[30:33], v[30:31], off nt
	v_add_co_u32_e32 v38, vcc, s53, v50
	v_mov_b32_e32 v77, v71
	s_nop 0
	v_addc_co_u32_e32 v39, vcc, 0, v51, vcc
	v_add_co_u32_e32 v46, vcc, s56, v50
	v_mov_b32_e32 v106, v71
	s_nop 0
	v_addc_co_u32_e32 v47, vcc, 0, v51, vcc
	global_load_dwordx4 v[34:37], v[38:39], off offset:-4096 nt
	s_nop 0
	global_load_dwordx4 v[38:41], v[38:39], off nt
	s_nop 0
	global_load_dwordx4 v[42:45], v[46:47], off offset:-4096 nt
	s_nop 0
	global_load_dwordx4 v[46:49], v[46:47], off nt
	v_add_co_u32_e32 v54, vcc, s57, v50
	v_mov_b32_e32 v75, v71
	s_nop 0
	v_addc_co_u32_e32 v55, vcc, 0, v51, vcc
	v_add_co_u32_e32 v62, vcc, s58, v50
	s_add_u32 s24, s5, s24
	s_nop 0
	v_addc_co_u32_e32 v63, vcc, 0, v51, vcc
	global_load_dwordx4 v[50:53], v[54:55], off offset:-4096 nt
	s_nop 0
	global_load_dwordx4 v[54:57], v[54:55], off nt
	s_nop 0
	global_load_dwordx4 v[58:61], v[62:63], off offset:-4096 nt
	s_nop 0
	global_load_dwordx4 v[62:65], v[62:63], off nt
	s_addc_u32 s25, s22, 0
	s_waitcnt vmcnt(15)
	v_mul_f32_e32 v3, 0x42800000, v3
	v_mul_f32_e32 v4, 0x42800000, v4
	v_mul_f32_e32 v5, 0x42800000, v5
	v_mul_f32_e32 v2, 0x42800000, v2
	s_waitcnt vmcnt(14)
	v_mul_f32_e32 v7, 0x42800000, v7
	v_mul_f32_e32 v8, 0x42800000, v8
	v_mul_f32_e32 v9, 0x42800000, v9
	v_cvt_pk_fp8_f32 v76, v3, v7
	v_cvt_pk_fp8_f32 v77, v4, v8
	v_cvt_pk_fp8_f32 v106, v5, v9
	v_mov_b32_e32 v5, v71
	v_mul_f32_e32 v6, 0x42800000, v6
	s_waitcnt vmcnt(11)
	v_mul_f32_e32 v3, 0x42800000, v19
	s_waitcnt vmcnt(10)
	v_mul_f32_e32 v4, 0x42800000, v23
	v_cvt_pk_fp8_f32 v5, v3, v4
	v_mul_f32_e32 v18, 0x42800000, v18
	v_mul_f32_e32 v22, 0x42800000, v22
	v_cvt_pk_fp8_f32 v75, v2, v6
	v_mov_b32_e32 v2, v71
	v_cvt_pk_fp8_f32 v2, v18, v22
	s_waitcnt vmcnt(9)
	v_mul_f32_e32 v3, 0x42800000, v27
	s_waitcnt vmcnt(8)
	v_mul_f32_e32 v4, 0x42800000, v31
	v_cvt_pk_fp8_f32 v5, v3, v4 op_sel:[0,0,1]
	v_mul_f32_e32 v3, 0x42800000, v20
	v_mul_f32_e32 v4, 0x42800000, v24
	v_mov_b32_e32 v8, v71
	v_cvt_pk_fp8_f32 v8, v3, v4
	v_mul_f32_e32 v3, 0x42800000, v21
	v_mul_f32_e32 v4, 0x42800000, v25
	v_mov_b32_e32 v9, v71
	v_mul_f32_e32 v10, 0x42800000, v10
	v_mul_f32_e32 v14, 0x42800000, v14
	v_mul_f32_e32 v26, 0x42800000, v26
	v_mul_f32_e32 v30, 0x42800000, v30
	v_cvt_pk_fp8_f32 v9, v3, v4
	v_mul_f32_e32 v11, 0x42800000, v11
	v_mul_f32_e32 v15, 0x42800000, v15
	v_cvt_pk_fp8_f32 v75, v10, v14 op_sel:[0,0,1]
	v_cvt_pk_fp8_f32 v2, v26, v30 op_sel:[0,0,1]
	v_mul_f32_e32 v12, 0x42800000, v12
	v_mul_f32_e32 v16, 0x42800000, v16
	v_cvt_pk_fp8_f32 v76, v11, v15 op_sel:[0,0,1]
	v_mul_f32_e32 v6, 0x42800000, v28
	v_mul_f32_e32 v7, 0x42800000, v32
	v_mul_f32_e32 v13, 0x42800000, v13
	v_mul_f32_e32 v17, 0x42800000, v17
	v_cvt_pk_fp8_f32 v77, v12, v16 op_sel:[0,0,1]
	v_cvt_pk_fp8_f32 v8, v6, v7 op_sel:[0,0,1]
	v_mul_f32_e32 v3, 0x42800000, v29
	v_mul_f32_e32 v4, 0x42800000, v33
	v_cvt_pk_fp8_f32 v106, v13, v17 op_sel:[0,0,1]
	v_cvt_pk_fp8_f32 v9, v3, v4 op_sel:[0,0,1]
	ds_write2_b32 v83, v75, v2 offset1:8
	ds_write2_b32 v83, v76, v5 offset0:33 offset1:41
	ds_write2_b32 v83, v77, v8 offset0:66 offset1:74
	ds_write2_b32 v83, v106, v9 offset0:99 offset1:107
	s_waitcnt vmcnt(7)
	v_mul_f32_e32 v2, 0x42800000, v34
	s_waitcnt vmcnt(6)
	v_mul_f32_e32 v3, 0x42800000, v38
	v_mov_b32_e32 v6, v71
	v_cvt_pk_fp8_f32 v6, v2, v3
	v_mul_f32_e32 v2, 0x42800000, v35
	v_mul_f32_e32 v3, 0x42800000, v39
	v_mov_b32_e32 v7, v71
	v_cvt_pk_fp8_f32 v7, v2, v3
	s_waitcnt vmcnt(5)
	v_mul_f32_e32 v2, 0x42800000, v43
	s_waitcnt vmcnt(4)
	v_mul_f32_e32 v3, 0x42800000, v47
	v_mov_b32_e32 v8, v71
	v_cvt_pk_fp8_f32 v7, v2, v3 op_sel:[0,0,1]
	v_mul_f32_e32 v2, 0x42800000, v36
	v_mul_f32_e32 v3, 0x42800000, v40
	v_cvt_pk_fp8_f32 v8, v2, v3
	v_mul_f32_e32 v2, 0x42800000, v37
	v_mul_f32_e32 v3, 0x42800000, v41
	v_mov_b32_e32 v9, v71
	v_cvt_pk_fp8_f32 v9, v2, v3
	v_mul_f32_e32 v2, 0x42800000, v45
	v_mul_f32_e32 v3, 0x42800000, v49
	v_mov_b32_e32 v10, v71
	v_cvt_pk_fp8_f32 v9, v2, v3 op_sel:[0,0,1]
	s_waitcnt vmcnt(3)
	v_mul_f32_e32 v2, 0x42800000, v50
	s_waitcnt vmcnt(2)
	v_mul_f32_e32 v3, 0x42800000, v54
	v_cvt_pk_fp8_f32 v10, v2, v3
	v_mul_f32_e32 v2, 0x42800000, v51
	v_mul_f32_e32 v3, 0x42800000, v55
	v_mov_b32_e32 v11, v71
	v_cvt_pk_fp8_f32 v11, v2, v3
	s_waitcnt vmcnt(1)
	v_mul_f32_e32 v2, 0x42800000, v59
	s_waitcnt vmcnt(0)
	v_mul_f32_e32 v3, 0x42800000, v63
	v_mul_f32_e32 v4, 0x42800000, v42
	v_mul_f32_e32 v5, 0x42800000, v46
	v_cvt_pk_fp8_f32 v11, v2, v3 op_sel:[0,0,1]
	v_mul_f32_e32 v2, 0x42800000, v52
	v_mul_f32_e32 v3, 0x42800000, v56
	v_mov_b32_e32 v12, v71
	v_cvt_pk_fp8_f32 v6, v4, v5 op_sel:[0,0,1]
	v_mul_f32_e32 v4, 0x42800000, v44
	v_mul_f32_e32 v5, 0x42800000, v48
	v_cvt_pk_fp8_f32 v12, v2, v3
	v_mul_f32_e32 v2, 0x42800000, v53
	v_mul_f32_e32 v3, 0x42800000, v57
	v_mov_b32_e32 v13, v71
	v_cvt_pk_fp8_f32 v8, v4, v5 op_sel:[0,0,1]
	v_mul_f32_e32 v4, 0x42800000, v58
	v_mul_f32_e32 v5, 0x42800000, v62
	v_cvt_pk_fp8_f32 v13, v2, v3
	v_cvt_pk_fp8_f32 v10, v4, v5 op_sel:[0,0,1]
	v_mul_f32_e32 v4, 0x42800000, v60
	v_mul_f32_e32 v5, 0x42800000, v64
	v_cvt_pk_fp8_f32 v12, v4, v5 op_sel:[0,0,1]
	v_mul_f32_e32 v2, 0x42800000, v61
	v_mul_f32_e32 v3, 0x42800000, v65
	v_cvt_pk_fp8_f32 v13, v2, v3 op_sel:[0,0,1]
	ds_write2_b32 v83, v6, v10 offset0:16 offset1:24
	ds_write2_b32 v83, v7, v11 offset0:49 offset1:57
	ds_write2_b32 v83, v8, v12 offset0:82 offset1:90
	ds_write2_b32 v83, v9, v13 offset0:115 offset1:123
	s_waitcnt lgkmcnt(0)
	ds_read2_b32 v[2:3], v84 offset1:1
	ds_read2_b32 v[4:5], v84 offset0:2 offset1:3
	v_or_b32_e32 v6, s4, v1
	v_lshl_add_u64 v[10:11], s[24:25], 0, v[72:73]
	v_lshlrev_b32_e32 v6, 10, v6
	v_mov_b32_e32 v7, v71
	v_lshl_add_u64 v[12:13], v[10:11], 0, v[6:7]
	ds_read2_b32 v[6:7], v85 offset1:1
	ds_read2_b32 v[8:9], v86 offset1:1
	s_waitcnt lgkmcnt(2)
	global_store_dwordx4 v[12:13], v[2:5], off sc1 nt
	s_nop 1
	v_or_b32_e32 v2, s4, v69
	v_lshlrev_b32_e32 v2, 10, v2
	v_mov_b32_e32 v3, v71
	v_lshl_add_u64 v[2:3], v[10:11], 0, v[2:3]
	s_waitcnt lgkmcnt(0)
	global_store_dwordx4 v[2:3], v[6:9], off sc1 nt
	ds_read2_b32 v[2:3], v87 offset1:1
	ds_read2_b32 v[4:5], v88 offset1:1
	v_or_b32_e32 v6, s4, v78
	v_lshlrev_b32_e32 v6, 10, v6
	v_mov_b32_e32 v7, v71
	v_lshl_add_u64 v[12:13], v[10:11], 0, v[6:7]
	ds_read2_b32 v[6:7], v89 offset1:1
	ds_read2_b32 v[8:9], v90 offset1:1
	s_waitcnt lgkmcnt(2)
	global_store_dwordx4 v[12:13], v[2:5], off sc1 nt
	s_nop 1
	v_or_b32_e32 v2, s4, v79
	v_lshlrev_b32_e32 v2, 10, v2
	v_mov_b32_e32 v3, v71
	v_lshl_add_u64 v[2:3], v[10:11], 0, v[2:3]
	s_waitcnt lgkmcnt(0)
	global_store_dwordx4 v[2:3], v[6:9], off sc1 nt
	s_waitcnt lgkmcnt(0)
.Lp0_w2_skip:
	s_mov_b64 s[4:5], 0
.LBB0_15:
	s_andn2_b64 vcc, exec, s[4:5]
	s_cbranch_vccnz .LBB0_17
	s_cmpk_lg_i32 s16, 0x800
	s_cbranch_scc1 .Lp0_w1_do
	s_cmp_gt_u32 s73, 0x61ff
	s_cbranch_scc1 .LBB0_17

.LBB0_1061:
	v_mov_b32_e32 v2, v243
	s_nop 15
	s_nop 15
	s_lshl_b32 s23, s51, 8
	v_readfirstlane_b32 s21, v2
	s_ashr_i32 s25, s21, 2
	s_andn2_b32 s25, s25, 63
	s_lshr_b32 s21, s21, 1
	s_add_i32 s25, s25, s23
	s_lshl_b32 s23, s76, 7
	s_and_b32 s21, s21, 0x60
	v_and_or_b32 v6, v2, 15, s25
	s_or_b32 s21, s21, s23
	v_lshrrev_b32_e32 v2, 1, v2
	v_and_or_b32 v4, v2, 24, s21
	s_waitcnt vmcnt(8)
	s_mov_b32 s32, 0
	s_cmp_gt_u32 s74, 2
	s_cbranch_scc1 .Lcg_skip_i
	s_cmp_gt_u32 s51, 0xff
	s_cbranch_scc1 .Lcg_skip_i
	s_load_dword s98, s[0:1], 0xb0
	s_load_dwordx2 s[80:81], s[0:1], 0x78
	s_load_dwordx2 s[82:83], s[0:1], 0xa0
	v_readlane_b32 s84, v255, 7
	v_readfirstlane_b32 s85, v0
	s_lshr_b32 s85, s85, 6
	s_lshl_b32 s84, s84, 3
	s_add_i32 s84, s84, s85
	s_lshr_b32 s85, s51, 5
	s_lshl_b32 s85, s85, 11
	s_add_i32 s85, s85, s84
	s_lshr_b32 s84, s85, 9
	s_add_i32 s99, s74, 1
	s_lshl_b32 s99, s99, 5
	s_add_i32 s84, s84, s99
	s_bfe_u32 s99, s85, 0x30006
	s_and_b32 s85, s85, 63
	s_lshl_b32 s92, s84, 22
	s_lshl_b32 s93, s99, 19
	s_add_u32 s92, s92, s93
	s_lshl_b32 s93, s85, 6
	s_add_u32 s100, s92, s93
	s_lshl_b32 s92, s84, 20
	s_lshl_b32 s93, s85, 14
	s_add_u32 s92, s92, s93
	s_lshl_b32 s93, s99, 7
	s_add_u32 s92, s92, s93
	s_add_u32 s92, s92, 0x21f00000
	s_waitcnt lgkmcnt(0)
	s_cmpk_lg_i32 s98, 0x100
	s_cbranch_scc1 .Lcg_skip_i
	s_add_u32 s80, s80, s100
	s_addc_u32 s81, s81, 0
	s_add_u32 s82, s82, s92
	s_addc_u32 s83, s83, 0
	v_and_b32_e32 v56, 63, v0
	v_lshrrev_b32_e32 v57, 2, v56
	v_and_b32_e32 v56, 3, v56
	v_lshlrev_b32_e32 v57, 14, v57
	v_lshl_or_b32 v56, v56, 4, v57
	global_load_dwordx4 v[24:27], v56, s[80:81] nt
	v_add_u32_e32 v57, 0x1000, v56
	global_load_dwordx4 v[28:31], v57, s[80:81] nt
	v_add_u32_e32 v57, 0x2000, v56
	global_load_dwordx4 v[32:35], v57, s[80:81] nt
	v_add_u32_e32 v57, 0x3000, v56
	global_load_dwordx4 v[36:39], v57, s[80:81] nt
	v_add_u32_e32 v57, 0x40000, v56
	global_load_dwordx4 v[40:43], v57, s[80:81] nt
	v_add_u32_e32 v57, 0x41000, v56
	global_load_dwordx4 v[44:47], v57, s[80:81] nt
	v_add_u32_e32 v57, 0x42000, v56
	global_load_dwordx4 v[48:51], v57, s[80:81] nt
	v_add_u32_e32 v57, 0x43000, v56
	global_load_dwordx4 v[52:55], v57, s[80:81] nt
	s_mov_b32 s32, 1
.Lcg_skip_i:
	v_pk_fma_f32 v[2:3], v[210:211], s[50:51], v[78:79] op_sel_hi:[1,0,1]
	v_pk_fma_f32 v[16:17], v[206:207], s[50:51], v[82:83] op_sel_hi:[1,0,1]
	v_min_f32_e32 v2, 0x40e00000, v2
	v_mul_f32_e32 v8, 0xc01d265f, v2
	v_min_f32_e32 v3, 0x40e00000, v3
	v_exp_f32_e32 v10, v8
	v_mul_f32_e32 v8, 0xc01d265f, v3
	v_exp_f32_e32 v11, v8
	v_pk_fma_f32 v[8:9], v[212:213], s[50:51], v[80:81] op_sel_hi:[1,0,1]
	v_add_f32_e32 v10, 1.0, v10
	v_rcp_f32_e32 v10, v10
	v_add_f32_e32 v11, 1.0, v11
	v_rcp_f32_e32 v11, v11
	v_min_f32_e32 v8, 0x40e00000, v8
	v_min_f32_e32 v9, 0x40e00000, v9
	v_mul_f32_e32 v12, 0xc01d265f, v8
	v_mul_f32_e32 v13, 0xc01d265f, v9
	v_exp_f32_e32 v12, v12
	v_exp_f32_e32 v13, v13
	v_med3_f32 v16, v16, s71, v242
	v_med3_f32 v17, v17, s71, v242
	v_pk_fma_f32 v[14:15], v[208:209], s[50:51], v[84:85] op_sel_hi:[1,0,1]
	v_pk_add_f32 v[16:17], v[16:17], 1.0 op_sel_hi:[1,0]
	v_pk_mul_f32 v[2:3], v[2:3], v[10:11]
	v_med3_f32 v14, v14, s71, v242
	v_med3_f32 v15, v15, s71, v242
	v_pk_mul_f32 v[2:3], v[2:3], v[16:17]
	v_mov_b32_e32 v10, v215
	v_cvt_pk_fp8_f32 v10, v2, v3
	v_pk_add_f32 v[2:3], v[14:15], 1.0 op_sel_hi:[1,0]
	v_pk_fma_f32 v[14:15], v[202:203], s[50:51], v[70:71] op_sel_hi:[1,0,1]
	v_add_f32_e32 v12, 1.0, v12
	v_add_f32_e32 v13, 1.0, v13
	v_min_f32_e32 v14, 0x40e00000, v14
	v_rcp_f32_e32 v12, v12
	v_rcp_f32_e32 v13, v13
	v_min_f32_e32 v15, 0x40e00000, v15
	v_mul_f32_e32 v11, 0xc01d265f, v14
	v_exp_f32_e32 v11, v11
	v_mul_f32_e32 v16, 0xc01d265f, v15
	v_exp_f32_e32 v17, v16
	v_pk_mul_f32 v[8:9], v[8:9], v[12:13]
	v_pk_fma_f32 v[12:13], v[204:205], s[50:51], v[72:73] op_sel_hi:[1,0,1]
	v_add_f32_e32 v11, 1.0, v11
	v_min_f32_e32 v12, 0x40e00000, v12
	v_min_f32_e32 v13, 0x40e00000, v13
	v_rcp_f32_e32 v16, v11
	v_add_f32_e32 v11, 1.0, v17
	v_mul_f32_e32 v17, 0xc01d265f, v12
	v_exp_f32_e32 v18, v17
	v_mul_f32_e32 v17, 0xc01d265f, v13
	v_exp_f32_e32 v19, v17
	v_rcp_f32_e32 v17, v11
	v_pk_mul_f32 v[2:3], v[8:9], v[2:3]
	v_pk_fma_f32 v[8:9], v[198:199], s[50:51], v[74:75] op_sel_hi:[1,0,1]
	v_add_f32_e32 v11, 1.0, v18
	v_med3_f32 v8, v8, s71, v242
	v_med3_f32 v9, v9, s71, v242
	v_rcp_f32_e32 v18, v11
	v_add_f32_e32 v11, 1.0, v19
	v_pk_add_f32 v[8:9], v[8:9], 1.0 op_sel_hi:[1,0]
	v_rcp_f32_e32 v19, v11
	v_pk_mul_f32 v[14:15], v[14:15], v[16:17]
	v_mov_b32_e32 v11, v215
	v_pk_mul_f32 v[8:9], v[14:15], v[8:9]
	v_cvt_pk_fp8_f32 v10, v2, v3 op_sel:[0,0,1]
	v_pk_fma_f32 v[2:3], v[200:201], s[50:51], v[76:77] op_sel_hi:[1,0,1]
	v_cvt_pk_fp8_f32 v11, v8, v9
	v_med3_f32 v2, v2, s71, v242
	v_med3_f32 v3, v3, s71, v242
	v_pk_add_f32 v[2:3], v[2:3], 1.0 op_sel_hi:[1,0]
	v_pk_mul_f32 v[8:9], v[12:13], v[18:19]
	v_ashrrev_i32_e32 v7, 31, v6
	v_pk_mul_f32 v[2:3], v[8:9], v[2:3]
	v_ashrrev_i32_e32 v5, 31, v4
	v_cvt_pk_fp8_f32 v11, v2, v3 op_sel:[0,0,1]
	v_lshlrev_b64 v[2:3], 10, v[6:7]
	v_lshl_add_u64 v[2:3], s[14:15], 0, v[2:3]
	v_lshl_add_u64 v[2:3], v[2:3], 0, v[4:5]
	global_store_dwordx2 v[2:3], v[10:11], off
	v_pk_fma_f32 v[10:11], v[194:195], s[50:51], v[78:79] op_sel_hi:[1,0,1]
	v_pk_fma_f32 v[20:21], v[190:191], s[50:51], v[82:83] op_sel_hi:[1,0,1]
	v_min_f32_e32 v10, 0x40e00000, v10
	v_mul_f32_e32 v7, 0xc01d265f, v10
	v_min_f32_e32 v11, 0x40e00000, v11
	v_exp_f32_e32 v7, v7
	v_mul_f32_e32 v12, 0xc01d265f, v11
	v_exp_f32_e32 v15, v12
	v_pk_fma_f32 v[12:13], v[196:197], s[50:51], v[80:81] op_sel_hi:[1,0,1]
	v_add_f32_e32 v7, 1.0, v7
	v_min_f32_e32 v12, 0x40e00000, v12
	v_rcp_f32_e32 v14, v7
	v_add_f32_e32 v7, 1.0, v15
	v_mul_f32_e32 v15, 0xc01d265f, v12
	v_min_f32_e32 v13, 0x40e00000, v13
	v_exp_f32_e32 v16, v15
	v_mul_f32_e32 v15, 0xc01d265f, v13
	v_exp_f32_e32 v17, v15
	v_rcp_f32_e32 v15, v7
	v_med3_f32 v20, v20, s71, v242
	v_med3_f32 v21, v21, s71, v242
	v_pk_fma_f32 v[18:19], v[192:193], s[50:51], v[84:85] op_sel_hi:[1,0,1]
	v_pk_add_f32 v[20:21], v[20:21], 1.0 op_sel_hi:[1,0]
	v_pk_mul_f32 v[10:11], v[10:11], v[14:15]
	v_med3_f32 v18, v18, s71, v242
	v_med3_f32 v19, v19, s71, v242
	v_pk_mul_f32 v[10:11], v[10:11], v[20:21]
	v_mov_b32_e32 v14, v215
	v_add_f32_e32 v7, 1.0, v16
	v_cvt_pk_fp8_f32 v14, v10, v11
	v_pk_add_f32 v[10:11], v[18:19], 1.0 op_sel_hi:[1,0]
	v_pk_fma_f32 v[18:19], v[186:187], s[50:51], v[70:71] op_sel_hi:[1,0,1]
	v_rcp_f32_e32 v16, v7
	v_add_f32_e32 v7, 1.0, v17
	v_min_f32_e32 v18, 0x40e00000, v18
	v_rcp_f32_e32 v17, v7
	v_min_f32_e32 v19, 0x40e00000, v19
	v_mul_f32_e32 v7, 0xc01d265f, v18
	v_exp_f32_e32 v7, v7
	v_mul_f32_e32 v15, 0xc01d265f, v19
	v_exp_f32_e32 v15, v15
	v_pk_mul_f32 v[12:13], v[12:13], v[16:17]
	v_pk_fma_f32 v[16:17], v[188:189], s[50:51], v[72:73] op_sel_hi:[1,0,1]
	v_add_f32_e32 v7, 1.0, v7
	v_min_f32_e32 v16, 0x40e00000, v16
	v_min_f32_e32 v17, 0x40e00000, v17
	v_rcp_f32_e32 v20, v7
	v_add_f32_e32 v7, 1.0, v15
	v_mul_f32_e32 v15, 0xc01d265f, v16
	v_exp_f32_e32 v15, v15
	v_mul_f32_e32 v21, 0xc01d265f, v17
	v_exp_f32_e32 v23, v21
	v_rcp_f32_e32 v21, v7
	v_pk_mul_f32 v[10:11], v[12:13], v[10:11]
	v_pk_fma_f32 v[12:13], v[182:183], s[50:51], v[74:75] op_sel_hi:[1,0,1]
	v_add_f32_e32 v7, 1.0, v15
	v_med3_f32 v12, v12, s71, v242
	v_med3_f32 v13, v13, s71, v242
	v_rcp_f32_e32 v22, v7
	v_add_f32_e32 v7, 1.0, v23
	v_pk_add_f32 v[12:13], v[12:13], 1.0 op_sel_hi:[1,0]
	v_rcp_f32_e32 v23, v7
	v_pk_mul_f32 v[18:19], v[18:19], v[20:21]
	v_mov_b32_e32 v15, v215
	v_pk_mul_f32 v[12:13], v[18:19], v[12:13]
	v_cvt_pk_fp8_f32 v14, v10, v11 op_sel:[0,0,1]
	v_pk_fma_f32 v[10:11], v[184:185], s[50:51], v[76:77] op_sel_hi:[1,0,1]
	v_cvt_pk_fp8_f32 v15, v12, v13
	v_med3_f32 v10, v10, s71, v242
	v_med3_f32 v11, v11, s71, v242
	v_pk_add_f32 v[10:11], v[10:11], 1.0 op_sel_hi:[1,0]
	v_pk_mul_f32 v[12:13], v[16:17], v[22:23]
	v_or_b32_e32 v8, 16, v6
	v_pk_mul_f32 v[10:11], v[12:13], v[10:11]
	v_ashrrev_i32_e32 v9, 31, v8
	v_cvt_pk_fp8_f32 v15, v10, v11 op_sel:[0,0,1]
	v_pk_fma_f32 v[10:11], v[178:179], s[50:51], v[78:79] op_sel_hi:[1,0,1]
	v_lshlrev_b64 v[8:9], 10, v[8:9]
	v_min_f32_e32 v10, 0x40e00000, v10
	v_lshl_add_u64 v[8:9], s[14:15], 0, v[8:9]
	v_mul_f32_e32 v7, 0xc01d265f, v10
	v_min_f32_e32 v11, 0x40e00000, v11
	v_lshl_add_u64 v[8:9], v[8:9], 0, v[4:5]
	v_exp_f32_e32 v7, v7
	v_mul_f32_e32 v12, 0xc01d265f, v11
	global_store_dwordx2 v[8:9], v[14:15], off
	v_exp_f32_e32 v15, v12
	v_pk_fma_f32 v[12:13], v[180:181], s[50:51], v[80:81] op_sel_hi:[1,0,1]
	v_add_f32_e32 v7, 1.0, v7
	v_min_f32_e32 v12, 0x40e00000, v12
	v_rcp_f32_e32 v14, v7
	v_add_f32_e32 v7, 1.0, v15
	v_mul_f32_e32 v15, 0xc01d265f, v12
	v_min_f32_e32 v13, 0x40e00000, v13
	v_exp_f32_e32 v16, v15
	v_mul_f32_e32 v15, 0xc01d265f, v13
	v_exp_f32_e32 v17, v15
	v_rcp_f32_e32 v15, v7
	v_pk_fma_f32 v[20:21], v[174:175], s[50:51], v[82:83] op_sel_hi:[1,0,1]
	v_pk_fma_f32 v[18:19], v[176:177], s[50:51], v[84:85] op_sel_hi:[1,0,1]
	v_med3_f32 v20, v20, s71, v242
	v_med3_f32 v21, v21, s71, v242
	v_pk_add_f32 v[20:21], v[20:21], 1.0 op_sel_hi:[1,0]
	v_pk_mul_f32 v[10:11], v[10:11], v[14:15]
	v_med3_f32 v18, v18, s71, v242
	v_med3_f32 v19, v19, s71, v242
	v_pk_mul_f32 v[10:11], v[10:11], v[20:21]
	v_mov_b32_e32 v14, v215
	v_add_f32_e32 v7, 1.0, v16
	v_cvt_pk_fp8_f32 v14, v10, v11
	v_pk_add_f32 v[10:11], v[18:19], 1.0 op_sel_hi:[1,0]
	v_pk_fma_f32 v[18:19], v[170:171], s[50:51], v[70:71] op_sel_hi:[1,0,1]
	v_rcp_f32_e32 v16, v7
	v_add_f32_e32 v7, 1.0, v17
	v_min_f32_e32 v18, 0x40e00000, v18
	v_rcp_f32_e32 v17, v7
	v_min_f32_e32 v19, 0x40e00000, v19
	v_mul_f32_e32 v7, 0xc01d265f, v18
	v_exp_f32_e32 v7, v7
	v_mul_f32_e32 v15, 0xc01d265f, v19
	v_exp_f32_e32 v15, v15
	v_pk_mul_f32 v[12:13], v[12:13], v[16:17]
	v_pk_fma_f32 v[16:17], v[172:173], s[50:51], v[72:73] op_sel_hi:[1,0,1]
	v_add_f32_e32 v7, 1.0, v7
	v_min_f32_e32 v16, 0x40e00000, v16
	v_min_f32_e32 v17, 0x40e00000, v17
	v_rcp_f32_e32 v20, v7
	v_add_f32_e32 v7, 1.0, v15
	v_mul_f32_e32 v15, 0xc01d265f, v16
	v_exp_f32_e32 v15, v15
	v_mul_f32_e32 v21, 0xc01d265f, v17
	v_exp_f32_e32 v23, v21
	v_rcp_f32_e32 v21, v7
	v_pk_mul_f32 v[10:11], v[12:13], v[10:11]
	v_pk_fma_f32 v[12:13], v[166:167], s[50:51], v[74:75] op_sel_hi:[1,0,1]
	v_add_f32_e32 v7, 1.0, v15
	v_med3_f32 v12, v12, s71, v242
	v_med3_f32 v13, v13, s71, v242
	v_rcp_f32_e32 v22, v7
	v_add_f32_e32 v7, 1.0, v23
	v_pk_add_f32 v[12:13], v[12:13], 1.0 op_sel_hi:[1,0]
	v_rcp_f32_e32 v23, v7
	v_pk_mul_f32 v[18:19], v[18:19], v[20:21]
	v_mov_b32_e32 v15, v215
	v_pk_mul_f32 v[12:13], v[18:19], v[12:13]
	v_cvt_pk_fp8_f32 v14, v10, v11 op_sel:[0,0,1]
	v_pk_fma_f32 v[10:11], v[168:169], s[50:51], v[76:77] op_sel_hi:[1,0,1]
	v_cvt_pk_fp8_f32 v15, v12, v13
	v_med3_f32 v10, v10, s71, v242
	v_med3_f32 v11, v11, s71, v242
	v_pk_add_f32 v[10:11], v[10:11], 1.0 op_sel_hi:[1,0]
	v_pk_mul_f32 v[12:13], v[16:17], v[22:23]
	v_or_b32_e32 v8, 32, v6
	v_pk_mul_f32 v[10:11], v[12:13], v[10:11]
	v_ashrrev_i32_e32 v9, 31, v8
	v_cvt_pk_fp8_f32 v15, v10, v11 op_sel:[0,0,1]
	v_lshlrev_b64 v[8:9], 10, v[8:9]
	v_lshl_add_u64 v[8:9], s[14:15], 0, v[8:9]
	v_lshl_add_u64 v[8:9], v[8:9], 0, v[4:5]
	global_store_dwordx2 v[8:9], v[14:15], off
	v_pk_fma_f32 v[8:9], v[162:163], s[50:51], v[78:79] op_sel_hi:[1,0,1]
	v_pk_fma_f32 v[18:19], v[158:159], s[50:51], v[82:83] op_sel_hi:[1,0,1]
	v_min_f32_e32 v8, 0x40e00000, v8
	v_mul_f32_e32 v10, 0xc01d265f, v8
	v_min_f32_e32 v9, 0x40e00000, v9
	v_exp_f32_e32 v12, v10
	v_mul_f32_e32 v10, 0xc01d265f, v9
	v_exp_f32_e32 v13, v10
	v_pk_fma_f32 v[10:11], v[164:165], s[50:51], v[80:81] op_sel_hi:[1,0,1]
	v_add_f32_e32 v12, 1.0, v12
	v_rcp_f32_e32 v12, v12
	v_add_f32_e32 v13, 1.0, v13
	v_rcp_f32_e32 v13, v13
	v_min_f32_e32 v10, 0x40e00000, v10
	v_min_f32_e32 v11, 0x40e00000, v11
	v_mul_f32_e32 v14, 0xc01d265f, v10
	v_mul_f32_e32 v15, 0xc01d265f, v11
	v_exp_f32_e32 v14, v14
	v_exp_f32_e32 v15, v15
	v_med3_f32 v18, v18, s71, v242
	v_med3_f32 v19, v19, s71, v242
	v_pk_fma_f32 v[16:17], v[160:161], s[50:51], v[84:85] op_sel_hi:[1,0,1]
	v_pk_add_f32 v[18:19], v[18:19], 1.0 op_sel_hi:[1,0]
	v_pk_mul_f32 v[8:9], v[8:9], v[12:13]
	v_med3_f32 v16, v16, s71, v242
	v_med3_f32 v17, v17, s71, v242
	v_pk_mul_f32 v[8:9], v[8:9], v[18:19]
	v_mov_b32_e32 v12, v215
	v_cvt_pk_fp8_f32 v12, v8, v9
	v_pk_add_f32 v[8:9], v[16:17], 1.0 op_sel_hi:[1,0]
	v_pk_fma_f32 v[16:17], v[154:155], s[50:51], v[70:71] op_sel_hi:[1,0,1]
	v_add_f32_e32 v14, 1.0, v14
	v_add_f32_e32 v15, 1.0, v15
	v_min_f32_e32 v16, 0x40e00000, v16
	v_rcp_f32_e32 v14, v14
	v_rcp_f32_e32 v15, v15
	v_min_f32_e32 v17, 0x40e00000, v17
	v_mul_f32_e32 v13, 0xc01d265f, v16
	v_exp_f32_e32 v13, v13
	v_mul_f32_e32 v18, 0xc01d265f, v17
	v_exp_f32_e32 v19, v18
	v_pk_mul_f32 v[10:11], v[10:11], v[14:15]
	v_pk_fma_f32 v[14:15], v[156:157], s[50:51], v[72:73] op_sel_hi:[1,0,1]
	v_add_f32_e32 v13, 1.0, v13
	v_min_f32_e32 v14, 0x40e00000, v14
	v_min_f32_e32 v15, 0x40e00000, v15
	v_rcp_f32_e32 v18, v13
	v_add_f32_e32 v13, 1.0, v19
	v_mul_f32_e32 v19, 0xc01d265f, v14
	v_exp_f32_e32 v20, v19
	v_mul_f32_e32 v19, 0xc01d265f, v15
	v_exp_f32_e32 v21, v19
	v_rcp_f32_e32 v19, v13
	v_pk_mul_f32 v[8:9], v[10:11], v[8:9]
	v_pk_fma_f32 v[10:11], v[150:151], s[50:51], v[74:75] op_sel_hi:[1,0,1]
	v_add_f32_e32 v13, 1.0, v20
	v_med3_f32 v10, v10, s71, v242
	v_med3_f32 v11, v11, s71, v242
	v_rcp_f32_e32 v20, v13
	v_add_f32_e32 v13, 1.0, v21
	v_pk_add_f32 v[10:11], v[10:11], 1.0 op_sel_hi:[1,0]
	v_rcp_f32_e32 v21, v13
	v_pk_mul_f32 v[16:17], v[16:17], v[18:19]
	v_mov_b32_e32 v13, v215
	v_pk_mul_f32 v[10:11], v[16:17], v[10:11]
	v_cvt_pk_fp8_f32 v12, v8, v9 op_sel:[0,0,1]
	v_pk_fma_f32 v[8:9], v[152:153], s[50:51], v[76:77] op_sel_hi:[1,0,1]
	v_cvt_pk_fp8_f32 v13, v10, v11
	v_med3_f32 v8, v8, s71, v242
	v_med3_f32 v9, v9, s71, v242
	v_pk_add_f32 v[8:9], v[8:9], 1.0 op_sel_hi:[1,0]
	v_pk_mul_f32 v[10:11], v[14:15], v[20:21]
	v_or_b32_e32 v6, 48, v6
	v_pk_mul_f32 v[8:9], v[10:11], v[8:9]
	v_ashrrev_i32_e32 v7, 31, v6
	v_cvt_pk_fp8_f32 v13, v8, v9 op_sel:[0,0,1]
	v_lshlrev_b64 v[6:7], 10, v[6:7]
	v_lshl_add_u64 v[6:7], s[14:15], 0, v[6:7]
	v_lshl_add_u64 v[4:5], v[6:7], 0, v[4:5]
	global_store_dwordx2 v[4:5], v[12:13], off
	v_pk_fma_f32 v[4:5], v[146:147], s[50:51], v[78:79] op_sel_hi:[1,0,1]
	v_pk_fma_f32 v[14:15], v[142:143], s[50:51], v[82:83] op_sel_hi:[1,0,1]
	v_min_f32_e32 v4, 0x40e00000, v4
	v_mul_f32_e32 v6, 0xc01d265f, v4
	v_min_f32_e32 v5, 0x40e00000, v5
	v_exp_f32_e32 v8, v6
	v_mul_f32_e32 v6, 0xc01d265f, v5
	v_exp_f32_e32 v9, v6
	v_pk_fma_f32 v[6:7], v[148:149], s[50:51], v[80:81] op_sel_hi:[1,0,1]
	v_add_f32_e32 v8, 1.0, v8
	v_rcp_f32_e32 v8, v8
	v_add_f32_e32 v9, 1.0, v9
	v_rcp_f32_e32 v9, v9
	v_min_f32_e32 v6, 0x40e00000, v6
	v_min_f32_e32 v7, 0x40e00000, v7
	v_mul_f32_e32 v10, 0xc01d265f, v6
	v_mul_f32_e32 v11, 0xc01d265f, v7
	v_exp_f32_e32 v10, v10
	v_exp_f32_e32 v11, v11
	v_med3_f32 v14, v14, s71, v242
	v_med3_f32 v15, v15, s71, v242
	v_pk_fma_f32 v[12:13], v[144:145], s[50:51], v[84:85] op_sel_hi:[1,0,1]
	v_pk_add_f32 v[14:15], v[14:15], 1.0 op_sel_hi:[1,0]
	v_pk_mul_f32 v[4:5], v[4:5], v[8:9]
	v_med3_f32 v12, v12, s71, v242
	v_med3_f32 v13, v13, s71, v242
	v_pk_mul_f32 v[4:5], v[4:5], v[14:15]
	v_mov_b32_e32 v8, v215
	v_cvt_pk_fp8_f32 v8, v4, v5
	v_pk_add_f32 v[4:5], v[12:13], 1.0 op_sel_hi:[1,0]
	v_pk_fma_f32 v[12:13], v[138:139], s[50:51], v[70:71] op_sel_hi:[1,0,1]
	v_add_f32_e32 v10, 1.0, v10
	v_add_f32_e32 v11, 1.0, v11
	v_min_f32_e32 v12, 0x40e00000, v12
	v_rcp_f32_e32 v10, v10
	v_rcp_f32_e32 v11, v11
	v_min_f32_e32 v13, 0x40e00000, v13
	v_mul_f32_e32 v9, 0xc01d265f, v12
	v_exp_f32_e32 v9, v9
	v_mul_f32_e32 v14, 0xc01d265f, v13
	v_exp_f32_e32 v15, v14
	v_pk_mul_f32 v[6:7], v[6:7], v[10:11]
	v_pk_fma_f32 v[10:11], v[140:141], s[50:51], v[72:73] op_sel_hi:[1,0,1]
	v_add_f32_e32 v9, 1.0, v9
	v_min_f32_e32 v10, 0x40e00000, v10
	v_min_f32_e32 v11, 0x40e00000, v11
	v_rcp_f32_e32 v14, v9
	v_add_f32_e32 v9, 1.0, v15
	v_mul_f32_e32 v15, 0xc01d265f, v10
	v_exp_f32_e32 v16, v15
	v_mul_f32_e32 v15, 0xc01d265f, v11
	v_exp_f32_e32 v17, v15
	v_rcp_f32_e32 v15, v9
	v_pk_mul_f32 v[4:5], v[6:7], v[4:5]
	v_pk_fma_f32 v[6:7], v[134:135], s[50:51], v[74:75] op_sel_hi:[1,0,1]
	v_add_f32_e32 v9, 1.0, v16
	v_med3_f32 v6, v6, s71, v242
	v_med3_f32 v7, v7, s71, v242
	v_rcp_f32_e32 v16, v9
	v_add_f32_e32 v9, 1.0, v17
	v_pk_add_f32 v[6:7], v[6:7], 1.0 op_sel_hi:[1,0]
	v_rcp_f32_e32 v17, v9
	v_pk_mul_f32 v[12:13], v[12:13], v[14:15]
	v_mov_b32_e32 v9, v215
	v_pk_mul_f32 v[6:7], v[12:13], v[6:7]
	v_cvt_pk_fp8_f32 v8, v4, v5 op_sel:[0,0,1]
	v_pk_fma_f32 v[4:5], v[136:137], s[50:51], v[76:77] op_sel_hi:[1,0,1]
	v_cvt_pk_fp8_f32 v9, v6, v7
	v_med3_f32 v4, v4, s71, v242
	v_med3_f32 v5, v5, s71, v242
	v_pk_add_f32 v[4:5], v[4:5], 1.0 op_sel_hi:[1,0]
	v_pk_mul_f32 v[6:7], v[10:11], v[16:17]
	v_pk_fma_f32 v[14:15], v[126:127], s[50:51], v[82:83] op_sel_hi:[1,0,1]
	v_pk_mul_f32 v[4:5], v[6:7], v[4:5]
	v_med3_f32 v14, v14, s71, v242
	v_cvt_pk_fp8_f32 v9, v4, v5 op_sel:[0,0,1]
	v_add_co_u32_e32 v4, vcc, s2, v2
	v_med3_f32 v15, v15, s71, v242
	s_nop 0
	v_addc_co_u32_e32 v5, vcc, 0, v3, vcc
	global_store_dwordx2 v[4:5], v[8:9], off
	v_pk_fma_f32 v[4:5], v[130:131], s[50:51], v[78:79] op_sel_hi:[1,0,1]
	v_pk_fma_f32 v[12:13], v[128:129], s[50:51], v[84:85] op_sel_hi:[1,0,1]
	v_min_f32_e32 v4, 0x40e00000, v4
	v_mul_f32_e32 v6, 0xc01d265f, v4
	v_min_f32_e32 v5, 0x40e00000, v5
	v_exp_f32_e32 v8, v6
	v_mul_f32_e32 v6, 0xc01d265f, v5
	v_exp_f32_e32 v9, v6
	v_pk_fma_f32 v[6:7], v[132:133], s[50:51], v[80:81] op_sel_hi:[1,0,1]
	v_add_f32_e32 v8, 1.0, v8
	v_rcp_f32_e32 v8, v8
	v_add_f32_e32 v9, 1.0, v9
	v_rcp_f32_e32 v9, v9
	v_min_f32_e32 v6, 0x40e00000, v6
	v_min_f32_e32 v7, 0x40e00000, v7
	v_mul_f32_e32 v10, 0xc01d265f, v6
	v_mul_f32_e32 v11, 0xc01d265f, v7
	v_exp_f32_e32 v10, v10
	v_exp_f32_e32 v11, v11
	v_pk_add_f32 v[14:15], v[14:15], 1.0 op_sel_hi:[1,0]
	v_pk_mul_f32 v[4:5], v[4:5], v[8:9]
	v_med3_f32 v12, v12, s71, v242
	v_med3_f32 v13, v13, s71, v242
	v_pk_mul_f32 v[4:5], v[4:5], v[14:15]
	v_mov_b32_e32 v8, v215
	v_cvt_pk_fp8_f32 v8, v4, v5
	v_pk_add_f32 v[4:5], v[12:13], 1.0 op_sel_hi:[1,0]
	v_pk_fma_f32 v[12:13], v[122:123], s[50:51], v[70:71] op_sel_hi:[1,0,1]
	v_add_f32_e32 v10, 1.0, v10
	v_add_f32_e32 v11, 1.0, v11
	v_min_f32_e32 v12, 0x40e00000, v12
	v_rcp_f32_e32 v10, v10
	v_rcp_f32_e32 v11, v11
	v_min_f32_e32 v13, 0x40e00000, v13
	v_mul_f32_e32 v9, 0xc01d265f, v12
	v_exp_f32_e32 v9, v9
	v_mul_f32_e32 v14, 0xc01d265f, v13
	v_exp_f32_e32 v15, v14
	v_pk_mul_f32 v[6:7], v[6:7], v[10:11]
	v_pk_fma_f32 v[10:11], v[124:125], s[50:51], v[72:73] op_sel_hi:[1,0,1]
	v_add_f32_e32 v9, 1.0, v9
	v_min_f32_e32 v10, 0x40e00000, v10
	v_min_f32_e32 v11, 0x40e00000, v11
	v_rcp_f32_e32 v14, v9
	v_add_f32_e32 v9, 1.0, v15
	v_mul_f32_e32 v15, 0xc01d265f, v10
	v_exp_f32_e32 v16, v15
	v_mul_f32_e32 v15, 0xc01d265f, v11
	v_exp_f32_e32 v17, v15
	v_rcp_f32_e32 v15, v9
	v_pk_mul_f32 v[4:5], v[6:7], v[4:5]
	v_pk_fma_f32 v[6:7], v[118:119], s[50:51], v[74:75] op_sel_hi:[1,0,1]
	v_add_f32_e32 v9, 1.0, v16
	v_med3_f32 v6, v6, s71, v242
	v_med3_f32 v7, v7, s71, v242
	v_rcp_f32_e32 v16, v9
	v_add_f32_e32 v9, 1.0, v17
	v_pk_add_f32 v[6:7], v[6:7], 1.0 op_sel_hi:[1,0]
	v_rcp_f32_e32 v17, v9
	v_pk_mul_f32 v[12:13], v[12:13], v[14:15]
	v_mov_b32_e32 v9, v215
	v_pk_mul_f32 v[6:7], v[12:13], v[6:7]
	v_cvt_pk_fp8_f32 v8, v4, v5 op_sel:[0,0,1]
	v_pk_fma_f32 v[4:5], v[120:121], s[50:51], v[76:77] op_sel_hi:[1,0,1]
	v_cvt_pk_fp8_f32 v9, v6, v7
	v_med3_f32 v4, v4, s71, v242
	v_med3_f32 v5, v5, s71, v242
	v_pk_add_f32 v[4:5], v[4:5], 1.0 op_sel_hi:[1,0]
	v_pk_mul_f32 v[6:7], v[10:11], v[16:17]
	s_mov_b32 s21, 0x24000
	v_pk_mul_f32 v[4:5], v[6:7], v[4:5]
	v_pk_fma_f32 v[14:15], v[110:111], s[50:51], v[82:83] op_sel_hi:[1,0,1]
	v_cvt_pk_fp8_f32 v9, v4, v5 op_sel:[0,0,1]
	v_add_co_u32_e32 v4, vcc, s21, v2
	v_med3_f32 v14, v14, s71, v242
	s_nop 0
	v_addc_co_u32_e32 v5, vcc, 0, v3, vcc
	global_store_dwordx2 v[4:5], v[8:9], off
	v_pk_fma_f32 v[4:5], v[114:115], s[50:51], v[78:79] op_sel_hi:[1,0,1]
	v_med3_f32 v15, v15, s71, v242
	v_min_f32_e32 v4, 0x40e00000, v4
	v_mul_f32_e32 v6, 0xc01d265f, v4
	v_min_f32_e32 v5, 0x40e00000, v5
	v_exp_f32_e32 v8, v6
	v_mul_f32_e32 v6, 0xc01d265f, v5
	v_exp_f32_e32 v9, v6
	v_pk_fma_f32 v[6:7], v[116:117], s[50:51], v[80:81] op_sel_hi:[1,0,1]
	v_add_f32_e32 v8, 1.0, v8
	v_rcp_f32_e32 v8, v8
	v_add_f32_e32 v9, 1.0, v9
	v_rcp_f32_e32 v9, v9
	v_min_f32_e32 v6, 0x40e00000, v6
	v_min_f32_e32 v7, 0x40e00000, v7
	v_mul_f32_e32 v10, 0xc01d265f, v6
	v_mul_f32_e32 v11, 0xc01d265f, v7
	v_exp_f32_e32 v10, v10
	v_exp_f32_e32 v11, v11
	v_pk_fma_f32 v[12:13], v[112:113], s[50:51], v[84:85] op_sel_hi:[1,0,1]
	v_pk_add_f32 v[14:15], v[14:15], 1.0 op_sel_hi:[1,0]
	v_pk_mul_f32 v[4:5], v[4:5], v[8:9]
	v_med3_f32 v12, v12, s71, v242
	v_med3_f32 v13, v13, s71, v242
	v_pk_mul_f32 v[4:5], v[4:5], v[14:15]
	v_mov_b32_e32 v8, v215
	v_cvt_pk_fp8_f32 v8, v4, v5
	v_pk_add_f32 v[4:5], v[12:13], 1.0 op_sel_hi:[1,0]
	v_pk_fma_f32 v[12:13], v[106:107], s[50:51], v[70:71] op_sel_hi:[1,0,1]
	v_add_f32_e32 v10, 1.0, v10
	v_add_f32_e32 v11, 1.0, v11
	v_min_f32_e32 v12, 0x40e00000, v12
	v_rcp_f32_e32 v10, v10
	v_rcp_f32_e32 v11, v11
	v_min_f32_e32 v13, 0x40e00000, v13
	v_mul_f32_e32 v9, 0xc01d265f, v12
	v_exp_f32_e32 v9, v9
	v_mul_f32_e32 v14, 0xc01d265f, v13
	v_exp_f32_e32 v15, v14
	v_pk_mul_f32 v[6:7], v[6:7], v[10:11]
	v_pk_fma_f32 v[10:11], v[108:109], s[50:51], v[72:73] op_sel_hi:[1,0,1]
	v_add_f32_e32 v9, 1.0, v9
	v_min_f32_e32 v10, 0x40e00000, v10
	v_min_f32_e32 v11, 0x40e00000, v11
	v_rcp_f32_e32 v14, v9
	v_add_f32_e32 v9, 1.0, v15
	v_mul_f32_e32 v15, 0xc01d265f, v10
	v_exp_f32_e32 v16, v15
	v_mul_f32_e32 v15, 0xc01d265f, v11
	v_exp_f32_e32 v17, v15
	v_rcp_f32_e32 v15, v9
	v_pk_mul_f32 v[4:5], v[6:7], v[4:5]
	v_pk_fma_f32 v[6:7], v[102:103], s[50:51], v[74:75] op_sel_hi:[1,0,1]
	v_add_f32_e32 v9, 1.0, v16
	v_med3_f32 v6, v6, s71, v242
	v_med3_f32 v7, v7, s71, v242
	v_rcp_f32_e32 v16, v9
	v_add_f32_e32 v9, 1.0, v17
	v_pk_add_f32 v[6:7], v[6:7], 1.0 op_sel_hi:[1,0]
	v_rcp_f32_e32 v17, v9
	v_pk_mul_f32 v[12:13], v[12:13], v[14:15]
	v_mov_b32_e32 v9, v215
	v_pk_mul_f32 v[6:7], v[12:13], v[6:7]
	v_cvt_pk_fp8_f32 v8, v4, v5 op_sel:[0,0,1]
	v_pk_fma_f32 v[4:5], v[104:105], s[50:51], v[76:77] op_sel_hi:[1,0,1]
	v_cvt_pk_fp8_f32 v9, v6, v7
	v_med3_f32 v4, v4, s71, v242
	v_med3_f32 v5, v5, s71, v242
	v_pk_add_f32 v[4:5], v[4:5], 1.0 op_sel_hi:[1,0]
	v_pk_mul_f32 v[6:7], v[10:11], v[16:17]
	s_mov_b32 s21, 0x28000
	v_pk_mul_f32 v[4:5], v[6:7], v[4:5]
	v_pk_fma_f32 v[10:11], v[98:99], s[50:51], v[78:79] op_sel_hi:[1,0,1]
	v_cvt_pk_fp8_f32 v9, v4, v5 op_sel:[0,0,1]
	v_add_co_u32_e32 v4, vcc, s21, v2
	v_min_f32_e32 v10, 0x40e00000, v10
	v_min_f32_e32 v11, 0x40e00000, v11
	v_addc_co_u32_e32 v5, vcc, 0, v3, vcc
	v_mul_f32_e32 v12, 0xc01d265f, v10
	v_mul_f32_e32 v13, 0xc01d265f, v11
	global_store_dwordx2 v[4:5], v[8:9], off
	v_pk_fma_f32 v[8:9], v[100:101], s[50:51], v[80:81] op_sel_hi:[1,0,1]
	v_exp_f32_e32 v12, v12
	v_exp_f32_e32 v13, v13
	v_min_f32_e32 v8, 0x40e00000, v8
	v_min_f32_e32 v9, 0x40e00000, v9
	v_mul_f32_e32 v14, 0xc01d265f, v8
	v_mul_f32_e32 v15, 0xc01d265f, v9
	v_exp_f32_e32 v14, v14
	v_exp_f32_e32 v15, v15
	v_add_f32_e32 v12, 1.0, v12
	v_add_f32_e32 v13, 1.0, v13
	v_rcp_f32_e32 v12, v12
	v_rcp_f32_e32 v13, v13
	v_add_f32_e32 v14, 1.0, v14
	v_add_f32_e32 v15, 1.0, v15
	v_pk_fma_f32 v[6:7], v[94:95], s[50:51], v[82:83] op_sel_hi:[1,0,1]
	v_rcp_f32_e32 v14, v14
	v_rcp_f32_e32 v15, v15
	v_med3_f32 v6, v6, s71, v242
	v_med3_f32 v7, v7, s71, v242
	v_pk_mul_f32 v[10:11], v[10:11], v[12:13]
	v_pk_fma_f32 v[12:13], v[90:91], s[50:51], v[70:71] op_sel_hi:[1,0,1]
	v_pk_add_f32 v[6:7], v[6:7], 1.0 op_sel_hi:[1,0]
	v_min_f32_e32 v12, 0x40e00000, v12
	v_pk_mul_f32 v[6:7], v[10:11], v[6:7]
	v_mov_b32_e32 v10, v215
	v_min_f32_e32 v13, 0x40e00000, v13
	v_mul_f32_e32 v11, 0xc01d265f, v12
	v_cvt_pk_fp8_f32 v10, v6, v7
	v_pk_mul_f32 v[6:7], v[8:9], v[14:15]
	v_exp_f32_e32 v11, v11
	v_mul_f32_e32 v14, 0xc01d265f, v13
	v_exp_f32_e32 v15, v14
	v_pk_fma_f32 v[8:9], v[92:93], s[50:51], v[72:73] op_sel_hi:[1,0,1]
	v_add_f32_e32 v11, 1.0, v11
	v_min_f32_e32 v8, 0x40e00000, v8
	v_min_f32_e32 v9, 0x40e00000, v9
	v_rcp_f32_e32 v14, v11
	v_add_f32_e32 v11, 1.0, v15
	v_mul_f32_e32 v15, 0xc01d265f, v8
	v_exp_f32_e32 v16, v15
	v_mul_f32_e32 v15, 0xc01d265f, v9
	v_pk_fma_f32 v[4:5], v[96:97], s[50:51], v[84:85] op_sel_hi:[1,0,1]
	v_exp_f32_e32 v17, v15
	v_med3_f32 v4, v4, s71, v242
	v_med3_f32 v5, v5, s71, v242
	v_rcp_f32_e32 v15, v11
	v_pk_add_f32 v[4:5], v[4:5], 1.0 op_sel_hi:[1,0]
	v_add_f32_e32 v11, 1.0, v16
	v_pk_mul_f32 v[4:5], v[6:7], v[4:5]
	v_pk_fma_f32 v[6:7], v[86:87], s[50:51], v[74:75] op_sel_hi:[1,0,1]
	v_rcp_f32_e32 v16, v11
	v_med3_f32 v6, v6, s71, v242
	v_med3_f32 v7, v7, s71, v242
	v_add_f32_e32 v11, 1.0, v17
	v_pk_add_f32 v[6:7], v[6:7], 1.0 op_sel_hi:[1,0]
	v_rcp_f32_e32 v17, v11
	v_pk_mul_f32 v[12:13], v[12:13], v[14:15]
	v_mov_b32_e32 v11, v215
	v_pk_mul_f32 v[6:7], v[12:13], v[6:7]
	v_cvt_pk_fp8_f32 v10, v4, v5 op_sel:[0,0,1]
	v_pk_fma_f32 v[4:5], v[88:89], s[50:51], v[76:77] op_sel_hi:[1,0,1]
	v_cvt_pk_fp8_f32 v11, v6, v7
	v_med3_f32 v4, v4, s71, v242
	v_med3_f32 v5, v5, s71, v242
	v_pk_add_f32 v[4:5], v[4:5], 1.0 op_sel_hi:[1,0]
	v_pk_mul_f32 v[6:7], v[8:9], v[16:17]
	v_add_co_u32_e32 v2, vcc, 0x2c000, v2
	v_pk_mul_f32 v[4:5], v[6:7], v[4:5]
	s_nop 0
	v_addc_co_u32_e32 v3, vcc, 0, v3, vcc
	v_cvt_pk_fp8_f32 v11, v4, v5 op_sel:[0,0,1]
	s_and_b64 vcc, exec, s[4:5]
	s_mov_b64 s[4:5], -1
	global_store_dwordx2 v[2:3], v[10:11], off
	s_cmp_eq_u32 s32, 0
	s_cbranch_scc1 .Lcg_skip_f
	s_waitcnt vmcnt(8)
	s_mov_b32 s100, 0x42800000
	s_mov_b32 s101, 0x42800000
	v_pk_mul_f32 v[24:25], v[24:25], s[100:101]
	v_pk_mul_f32 v[26:27], v[26:27], s[100:101]
	v_pk_mul_f32 v[28:29], v[28:29], s[100:101]
	v_pk_mul_f32 v[30:31], v[30:31], s[100:101]
	v_pk_mul_f32 v[32:33], v[32:33], s[100:101]
	v_pk_mul_f32 v[34:35], v[34:35], s[100:101]
	v_pk_mul_f32 v[36:37], v[36:37], s[100:101]
	v_pk_mul_f32 v[38:39], v[38:39], s[100:101]
	v_pk_mul_f32 v[40:41], v[40:41], s[100:101]
	v_pk_mul_f32 v[42:43], v[42:43], s[100:101]
	v_pk_mul_f32 v[44:45], v[44:45], s[100:101]
	v_pk_mul_f32 v[46:47], v[46:47], s[100:101]
	v_pk_mul_f32 v[48:49], v[48:49], s[100:101]
	v_pk_mul_f32 v[50:51], v[50:51], s[100:101]
	v_pk_mul_f32 v[52:53], v[52:53], s[100:101]
	v_pk_mul_f32 v[54:55], v[54:55], s[100:101]
	v_cvt_pk_fp8_f32 v24, v24, v28
	v_cvt_pk_fp8_f32 v24, v32, v36 op_sel:[0,0,1]
	v_cvt_pk_fp8_f32 v25, v25, v29
	v_cvt_pk_fp8_f32 v25, v33, v37 op_sel:[0,0,1]
	v_cvt_pk_fp8_f32 v26, v26, v30
	v_cvt_pk_fp8_f32 v26, v34, v38 op_sel:[0,0,1]
	v_cvt_pk_fp8_f32 v27, v27, v31
	v_cvt_pk_fp8_f32 v27, v35, v39 op_sel:[0,0,1]
	v_cvt_pk_fp8_f32 v40, v40, v44
	v_cvt_pk_fp8_f32 v40, v48, v52 op_sel:[0,0,1]
	v_cvt_pk_fp8_f32 v41, v41, v45
	v_cvt_pk_fp8_f32 v41, v49, v53 op_sel:[0,0,1]
	v_cvt_pk_fp8_f32 v42, v42, v46
	v_cvt_pk_fp8_f32 v42, v50, v54 op_sel:[0,0,1]
	v_cvt_pk_fp8_f32 v43, v43, v47
	v_cvt_pk_fp8_f32 v43, v51, v55 op_sel:[0,0,1]
	v_readfirstlane_b32 s84, v0
	s_lshr_b32 s84, s84, 6
	s_mul_i32 s85, s84, 0x420
	s_add_i32 s85, s85, s53
	s_add_i32 s85, s85, 0x20800
	s_cmp_lt_u32 s84, 5
	s_cselect_b32 s84, 0, 0x4b60
	s_add_i32 s85, s85, s84
	v_and_b32_e32 v59, 63, v0
	v_and_b32_e32 v60, 1, v59
	v_mul_u32_u24_e32 v60, 0x84, v60
	v_lshrrev_b32_e32 v61, 2, v59
	v_add_u32_e32 v60, v60, v61
	v_lshl_add_u32 v60, v60, 2, s85
	v_lshrrev_b32_e32 v61, 3, v59
	v_mul_u32_u24_e32 v61, 33, v61
	v_and_b32_e32 v62, 7, v59
	v_lshl_add_u32 v61, v62, 2, v61
	v_lshl_add_u32 v61, v61, 2, s85
	v_lshrrev_b32_e32 v58, 3, v59
	v_lshlrev_b32_e32 v58, 10, v58
	v_lshl_or_b32 v58, v62, 4, v58
	v_add_u32_e32 v62, 0x2000, v58
	s_mov_b64 s[92:93], exec
	s_mov_b32 exec_lo, 0x33333333
	s_mov_b32 exec_hi, 0x33333333
	ds_write2_b32 v60, v24, v40 offset0:0 offset1:16
	ds_write2_b32 v60, v25, v41 offset0:33 offset1:49
	ds_write2_b32 v60, v26, v42 offset0:66 offset1:82
	ds_write2_b32 v60, v27, v43 offset0:99 offset1:115
	s_mov_b64 exec, s[92:93]
	s_waitcnt lgkmcnt(0)
	ds_read2_b32 v[28:29], v61 offset1:1
	ds_read2_b32 v[30:31], v61 offset0:2 offset1:3
	s_mov_b32 exec_lo, 0xcccccccc
	s_mov_b32 exec_hi, 0xcccccccc
	ds_write2_b32 v60, v24, v40 offset0:0 offset1:16
	ds_write2_b32 v60, v25, v41 offset0:33 offset1:49
	ds_write2_b32 v60, v26, v42 offset0:66 offset1:82
	ds_write2_b32 v60, v27, v43 offset0:99 offset1:115
	s_mov_b64 exec, s[92:93]
	s_waitcnt lgkmcnt(0)
	global_store_dwordx4 v58, v[28:31], s[82:83] sc1 nt
	ds_read2_b32 v[32:33], v61 offset1:1
	ds_read2_b32 v[34:35], v61 offset0:2 offset1:3
	s_waitcnt lgkmcnt(0)
	global_store_dwordx4 v62, v[32:35], s[82:83] sc1 nt
.Lcg_skip_f:
	s_cbranch_vccnz .LBB0_1049
	s_ashr_i32 s21, s20, 31
	s_lshl_b64 s[4:5], s[20:21], 13
	s_add_u32 s21, s40, s4
	s_addc_u32 s23, s57, s5
	s_lshl_b32 s4, s24, 7
	s_ashr_i32 s5, s4, 31
	s_lshl_b64 s[4:5], s[4:5], 2
	s_add_u32 s4, s21, s4
	s_addc_u32 s5, s23, s5
	s_add_u32 s4, s4, s60
	s_addc_u32 s5, s5, 0
	v_mov_b32_e32 v221, v215
	v_lshl_add_u64 v[2:3], s[4:5], 0, v[220:221]
	s_mov_b64 s[78:79], 0x1000
	v_lshl_add_u64 v[4:5], v[2:3], 0, s[78:79]
	v_add_co_u32_e32 v2, vcc, 0x1000, v2
	global_load_dwordx4 v[70:73], v220, s[4:5] offset:16
	global_load_dwordx4 v[78:81], v220, s[4:5]
	v_addc_co_u32_e32 v3, vcc, 0, v3, vcc
	global_load_dwordx4 v[82:85], v[2:3], off
	global_load_dwordx4 v[74:77], v[4:5], off offset:16
	s_andn2_b64 vcc, exec, s[12:13]
	s_cbranch_vccnz .LBB0_1048
	s_barrier
	s_branch .LBB0_1048
